# speedup vs baseline: 1.0261x; 1.0261x over previous
.LBB1_36:
	s_or_b64 exec, exec, s[6:7]
	s_lshl_b32 s0, s2, 12
	s_sub_i32 s1, 0x186a00, s0
	s_min_u32 s22, s1, 0x1000
	s_mov_b32 s1, 0
	s_lshl_b64 s[0:1], s[0:1], 2
	s_waitcnt lgkmcnt(0)
	s_add_u32 s8, s12, s0
	s_addc_u32 s9, s13, s1
	s_add_u32 s10, s14, s0
	s_addc_u32 s11, s15, s1
	v_cmp_gt_u32_e64 s[0:1], s22, v34
	v_mov_b32_e32 v2, 0
	v_mov_b32_e32 v10, 0
	v_mov_b32_e32 v11, 0
	v_mov_b32_e32 v12, 0
	v_mov_b32_e32 v13, 0
	v_mov_b32_e32 v16, 0
	v_mov_b32_e32 v17, 0
	v_mov_b32_e32 v14, 0
	v_mov_b32_e32 v15, 0
	s_barrier
	s_and_saveexec_b64 s[2:3], s[0:1]
	s_cbranch_execz .LBB1_38
	v_mov_b32_e32 v35, 0
	v_lshlrev_b64 v[4:5], 2, v[34:35]
	v_lshl_add_u64 v[6:7], s[8:9], 0, v[4:5]
	v_lshl_add_u64 v[4:5], s[10:11], 0, v[4:5]
	global_load_dwordx4 v[10:13], v[4:5], off nt
	global_load_dwordx4 v[14:17], v[6:7], off nt
.LBB1_38:
	s_or_b64 exec, exec, s[2:3]
	v_add_u32_e32 v36, 0x400, v34
	v_cmp_gt_u32_e64 s[2:3], s22, v36
	v_mov_b32_e32 v3, 0
	v_mov_b32_e32 v4, 0
	v_mov_b32_e32 v5, 0
	v_mov_b32_e32 v24, 0
	v_mov_b32_e32 v25, 0
	v_mov_b32_e32 v22, 0
	v_mov_b32_e32 v23, 0
	s_and_saveexec_b64 s[4:5], s[2:3]
	s_cbranch_execz .LBB1_40
	v_mov_b32_e32 v37, 0
	v_lshlrev_b64 v[2:3], 2, v[36:37]
	v_lshl_add_u64 v[8:9], s[10:11], 0, v[2:3]
	v_lshl_add_u64 v[6:7], s[8:9], 0, v[2:3]
	global_load_dwordx4 v[2:5], v[8:9], off nt
	global_load_dwordx4 v[22:25], v[6:7], off nt
.LBB1_40:
	s_or_b64 exec, exec, s[4:5]
	v_add_u32_e32 v8, 0x800, v34
	v_cmp_gt_u32_e64 s[4:5], s22, v8
	v_mov_b32_e32 v6, 0
	v_mov_b32_e32 v18, 0
	v_mov_b32_e32 v19, 0
	v_mov_b32_e32 v20, 0
	v_mov_b32_e32 v21, 0
	v_mov_b32_e32 v28, 0
	v_mov_b32_e32 v29, 0
	v_mov_b32_e32 v26, 0
	v_mov_b32_e32 v27, 0
	s_and_saveexec_b64 s[6:7], s[4:5]
	s_cbranch_execz .LBB1_42
	v_mov_b32_e32 v9, 0
	v_lshlrev_b64 v[8:9], 2, v[8:9]
	v_lshl_add_u64 v[30:31], s[8:9], 0, v[8:9]
	v_lshl_add_u64 v[8:9], s[10:11], 0, v[8:9]
	global_load_dwordx4 v[18:21], v[8:9], off nt
	global_load_dwordx4 v[26:29], v[30:31], off nt
.LBB1_42:
	s_or_b64 exec, exec, s[6:7]
	v_add_u32_e32 v38, 0xc00, v34
	v_cmp_gt_u32_e64 s[6:7], s22, v38
	v_mov_b32_e32 v7, 0
	v_mov_b32_e32 v8, 0
	v_mov_b32_e32 v9, 0
	v_mov_b32_e32 v32, 0
	v_mov_b32_e32 v33, 0
	v_mov_b32_e32 v30, 0
	v_mov_b32_e32 v31, 0
	s_and_saveexec_b64 s[12:13], s[6:7]
	s_cbranch_execz .LBB1_44
	v_mov_b32_e32 v39, 0
	v_lshlrev_b64 v[6:7], 2, v[38:39]
	v_lshl_add_u64 v[42:43], s[10:11], 0, v[6:7]
	v_lshl_add_u64 v[38:39], s[8:9], 0, v[6:7]
	global_load_dwordx4 v[6:9], v[42:43], off nt
	global_load_dwordx4 v[30:33], v[38:39], off nt
